# indexer scoring loop: next key tile's address math and loads fill the post-MFMA wait (no s_nop 11); DSA mask-word addresses by one 64-bit add each; on top of DSA table mask and trims
# baseline (speedup 1.0000x reference)
.LBB0_1077:
	v_lshl_add_u64 v[14:15], v[184:185], 0, s[54:55]
	s_mov_b64 s[38:39], 0xeb20000
	v_lshl_add_u64 v[2:3], v[14:15], 0, s[38:39]
	s_mov_b64 s[38:39], 0xeb28000
	v_add_u32_e32 v12, s29, v239
	v_lshl_add_u64 v[4:5], v[14:15], 0, s[38:39]
	global_load_dword v0, v[2:3], off
	global_load_dword v190, v[4:5], off
	global_load_dword v191, v[182:183], off offset:-4
	v_lshrrev_b32_e32 v2, v238, v211
	v_lshrrev_b32_e32 v3, v238, v213
	v_bfe_u32 v4, v2, 0, 4
	v_lshl_add_u32 v4, v4, 4, s100
	ds_read_b128 v[80:83], v4
	v_bfe_u32 v4, v2, 8, 4
	v_lshl_add_u32 v4, v4, 4, s100
	ds_read_b128 v[84:87], v4
	v_bfe_u32 v4, v2, 16, 4
	v_lshl_add_u32 v4, v4, 4, s100
	ds_read_b128 v[88:91], v4
	v_bfe_u32 v4, v2, 24, 4
	v_lshl_add_u32 v4, v4, 4, s100
	ds_read_b128 v[92:95], v4
	v_bfe_u32 v4, v3, 0, 4
	v_lshl_add_u32 v4, v4, 4, s100
	ds_read_b128 v[96:99], v4
	v_bfe_u32 v4, v3, 8, 4
	v_lshl_add_u32 v4, v4, 4, s100
	ds_read_b128 v[100:103], v4
	v_bfe_u32 v4, v3, 16, 4
	v_lshl_add_u32 v4, v4, 4, s100
	ds_read_b128 v[104:107], v4
	v_bfe_u32 v4, v3, 24, 4
	v_lshl_add_u32 v4, v4, 4, s100
	ds_read_b128 v[108:111], v4
	ds_read_b64_tr_b16 v[176:177], v12 offset:24576
	ds_read_b64_tr_b16 v[178:179], v12 offset:25088
	s_waitcnt lgkmcnt(6)
	v_mfma_f32_32x32x16_bf16 v[80:95], v[172:175], v[124:127], v[80:95]
	v_add_f32_e32 v2, v64, v65
	v_add_f32_e32 v2, v66, v2
	v_add_f32_e32 v2, v67, v2
	v_add_f32_e32 v2, v68, v2
	v_add_f32_e32 v2, v69, v2
	v_cvt_pk_bf16_f32 v140, v64, v65
	v_cvt_pk_bf16_f32 v141, v66, v67
	ds_read_b64_tr_b16 v[172:173], v12 offset:28672
	ds_read_b64_tr_b16 v[174:175], v12 offset:29184
	s_waitcnt lgkmcnt(4)
	v_mfma_f32_32x32x16_bf16 v[96:111], v[164:167], v[124:127], v[96:111]
	v_add_f32_e32 v2, v70, v2
	v_add_f32_e32 v2, v71, v2
	v_add_f32_e32 v2, v72, v2
	v_add_f32_e32 v2, v73, v2
	v_cvt_pk_bf16_f32 v142, v68, v69
	v_cvt_pk_bf16_f32 v143, v70, v71
	ds_read_b64_tr_b16 v[164:165], v12 offset:25600
	ds_read_b64_tr_b16 v[166:167], v12 offset:26112
	s_waitcnt lgkmcnt(11)
	v_mfma_f32_32x32x16_bf16 v[80:95], v[168:171], v[120:123], v[80:95]
	v_add_f32_e32 v2, v74, v2
	v_add_f32_e32 v2, v75, v2
	v_add_f32_e32 v2, v76, v2
	v_add_f32_e32 v2, v77, v2
	v_cvt_pk_bf16_f32 v136, v72, v73
	v_cvt_pk_bf16_f32 v137, v74, v75
	ds_read_b64_tr_b16 v[168:169], v12 offset:29696
	ds_read_b64_tr_b16 v[170:171], v12 offset:30208
	s_waitcnt lgkmcnt(12)
	v_mfma_f32_32x32x16_bf16 v[96:111], v[160:163], v[120:123], v[96:111]
	v_add_f32_e32 v2, v78, v2
	v_add_f32_e32 v2, v79, v2
	v_add_f32_e32 v2, v48, v2
	v_add_f32_e32 v2, v49, v2
	v_cvt_pk_bf16_f32 v138, v76, v77
	v_cvt_pk_bf16_f32 v139, v78, v79
	ds_read_b64_tr_b16 v[160:161], v12 offset:26624
	ds_read_b64_tr_b16 v[162:163], v12 offset:27136
	s_waitcnt lgkmcnt(13)
	v_mfma_f32_32x32x16_bf16 v[80:95], v[156:159], v[116:119], v[80:95]
	v_add_f32_e32 v2, v50, v2
	v_add_f32_e32 v2, v51, v2
	v_add_f32_e32 v2, v52, v2
	v_add_f32_e32 v6, v53, v2
	v_cvt_pk_bf16_f32 v132, v48, v49
	v_cvt_pk_bf16_f32 v133, v50, v51
	ds_read_b64_tr_b16 v[2:3], v12 offset:30720
	ds_read_b64_tr_b16 v[4:5], v12 offset:31232
	s_waitcnt lgkmcnt(14)
	v_mfma_f32_32x32x16_bf16 v[96:111], v[152:155], v[116:119], v[96:111]
	v_add_f32_e32 v6, v54, v6
	v_add_f32_e32 v6, v55, v6
	v_add_f32_e32 v6, v56, v6
	v_add_f32_e32 v10, v57, v6
	v_cvt_pk_bf16_f32 v134, v52, v53
	v_cvt_pk_bf16_f32 v135, v54, v55
	ds_read_b64_tr_b16 v[6:7], v12 offset:27648
	ds_read_b64_tr_b16 v[8:9], v12 offset:28160
	s_waitcnt lgkmcnt(14)
	v_mfma_f32_32x32x16_bf16 v[80:95], v[148:151], v[112:115], v[80:95]
	v_add_f32_e32 v10, v58, v10
	v_add_f32_e32 v10, v59, v10
	v_add_f32_e32 v10, v60, v10
	v_add_f32_e32 v48, v61, v10
	v_cvt_pk_bf16_f32 v128, v56, v57
	v_cvt_pk_bf16_f32 v129, v58, v59
	ds_read_b64_tr_b16 v[10:11], v12 offset:31744
	ds_read_b64_tr_b16 v[12:13], v12 offset:32256
	v_mfma_f32_32x32x16_bf16 v[96:111], v[144:147], v[112:115], v[96:111]
	v_add_f32_e32 v48, v62, v48
	v_add_f32_e32 v48, v63, v48
	v_cvt_pk_bf16_f32 v130, v60, v61
	v_cvt_pk_bf16_f32 v131, v62, v63
	v_lshl_add_u64 v[186:187], v[216:217], 0, s[54:55]
	v_lshl_add_u64 v[50:51], v[186:187], 0, s[20:21]
	s_add_i32 s29, s59, s63
	s_mov_b32 m0, s29
	s_nop 0
	global_load_lds_dwordx4 v[50:51], off
	v_lshl_add_u64 v[188:189], v[218:219], 0, s[54:55]
	v_lshl_add_u64 v[50:51], v[188:189], 0, s[24:25]
	s_add_i32 s29, s57, s62
	s_mov_b32 m0, s29
	s_nop 0
	global_load_lds_dwordx4 v[50:51], off
	s_waitcnt vmcnt(7)
	v_mul_f32_e32 v49, v201, v209
	v_cmp_nge_f32_e32 vcc, s73, v49
	v_cmp_neq_f32_e64 s[38:39], 0, v207
	s_or_b64 vcc, vcc, s[38:39]
	s_cmp_lg_u64 vcc, 0
	s_cselect_b64 s[38:39], -1, 0
	s_cbranch_vccz .LBB0_1079
	v_sub_f32_e32 v95, v95, v207
	v_sub_f32_e32 v94, v94, v207
	v_sub_f32_e32 v93, v93, v207
	v_sub_f32_e32 v92, v92, v207
	v_sub_f32_e32 v91, v91, v207
	v_sub_f32_e32 v90, v90, v207
	v_sub_f32_e32 v89, v89, v207
	v_sub_f32_e32 v88, v88, v207
	v_sub_f32_e32 v87, v87, v207
	v_sub_f32_e32 v86, v86, v207
	v_sub_f32_e32 v85, v85, v207
	v_sub_f32_e32 v84, v84, v207
	v_sub_f32_e32 v83, v83, v207
	v_sub_f32_e32 v82, v82, v207
	v_sub_f32_e32 v81, v81, v207
	v_sub_f32_e32 v80, v80, v207
	v_sub_f32_e32 v111, v111, v207
	v_sub_f32_e32 v110, v110, v207
	v_sub_f32_e32 v109, v109, v207
	v_sub_f32_e32 v108, v108, v207
	v_sub_f32_e32 v107, v107, v207
	v_sub_f32_e32 v106, v106, v207
	v_sub_f32_e32 v105, v105, v207
	v_sub_f32_e32 v104, v104, v207
	v_sub_f32_e32 v103, v103, v207
	v_sub_f32_e32 v102, v102, v207
	v_sub_f32_e32 v101, v101, v207
	v_sub_f32_e32 v100, v100, v207
	v_sub_f32_e32 v99, v99, v207
	v_sub_f32_e32 v98, v98, v207
	v_sub_f32_e32 v97, v97, v207
	v_sub_f32_e32 v96, v96, v207

.LBB0_1082:
	s_add_i32 s29, s57, 0x2000
	s_cmpk_lg_i32 s57, 0x4000
	s_cselect_b32 s65, s29, 0
	s_mov_b64 s[38:39], 0xeb30000
	v_add_u32_e32 v12, s59, v239
	v_lshl_add_u64 v[2:3], v[14:15], 0, s[38:39]
	global_load_dword v192, v[2:3], off
	s_mov_b64 s[38:39], 0xeb38000
	v_lshl_add_u64 v[2:3], v[14:15], 0, s[38:39]
	global_load_dword v14, v[2:3], off
	global_load_dword v209, v[182:183], off
	v_lshrrev_b32_e32 v2, v238, v0
	v_lshrrev_b32_e32 v3, v238, v190
	v_bfe_u32 v4, v2, 0, 4
	v_lshl_add_u32 v4, v4, 4, s100
	ds_read_b128 v[80:83], v4
	v_bfe_u32 v4, v2, 8, 4
	v_lshl_add_u32 v4, v4, 4, s100
	ds_read_b128 v[84:87], v4
	v_bfe_u32 v4, v2, 16, 4
	v_lshl_add_u32 v4, v4, 4, s100
	ds_read_b128 v[88:91], v4
	v_bfe_u32 v4, v2, 24, 4
	v_lshl_add_u32 v4, v4, 4, s100
	ds_read_b128 v[92:95], v4
	v_bfe_u32 v4, v3, 0, 4
	v_lshl_add_u32 v4, v4, 4, s100
	ds_read_b128 v[96:99], v4
	v_bfe_u32 v4, v3, 8, 4
	v_lshl_add_u32 v4, v4, 4, s100
	ds_read_b128 v[100:103], v4
	v_bfe_u32 v4, v3, 16, 4
	v_lshl_add_u32 v4, v4, 4, s100
	ds_read_b128 v[104:107], v4
	v_bfe_u32 v4, v3, 24, 4
	v_lshl_add_u32 v4, v4, 4, s100
	ds_read_b128 v[108:111], v4
	ds_read_b64_tr_b16 v[156:157], v12 offset:24576
	ds_read_b64_tr_b16 v[158:159], v12 offset:25088
	s_waitcnt lgkmcnt(6)
	v_mfma_f32_32x32x16_bf16 v[80:95], v[140:143], v[124:127], v[80:95]
	v_add_f32_e32 v2, v64, v65
	v_add_f32_e32 v2, v66, v2
	v_add_f32_e32 v2, v67, v2
	v_add_f32_e32 v2, v68, v2
	v_add_f32_e32 v2, v69, v2
	v_cvt_pk_bf16_f32 v140, v64, v65
	v_cvt_pk_bf16_f32 v141, v66, v67
	ds_read_b64_tr_b16 v[152:153], v12 offset:28672
	ds_read_b64_tr_b16 v[154:155], v12 offset:29184
	s_waitcnt lgkmcnt(4)
	v_mfma_f32_32x32x16_bf16 v[96:111], v[136:139], v[124:127], v[96:111]
	v_add_f32_e32 v2, v70, v2
	v_add_f32_e32 v2, v71, v2
	v_add_f32_e32 v2, v72, v2
	v_add_f32_e32 v2, v73, v2
	v_cvt_pk_bf16_f32 v142, v68, v69
	v_cvt_pk_bf16_f32 v143, v70, v71
	ds_read_b64_tr_b16 v[144:145], v12 offset:25600
	ds_read_b64_tr_b16 v[146:147], v12 offset:26112
	s_waitcnt lgkmcnt(11)
	v_mfma_f32_32x32x16_bf16 v[80:95], v[148:151], v[120:123], v[80:95]
	v_add_f32_e32 v2, v74, v2
	v_add_f32_e32 v2, v75, v2
	v_add_f32_e32 v2, v76, v2
	v_add_f32_e32 v2, v77, v2
	v_cvt_pk_bf16_f32 v136, v72, v73
	v_cvt_pk_bf16_f32 v137, v74, v75
	ds_read_b64_tr_b16 v[148:149], v12 offset:29696
	ds_read_b64_tr_b16 v[150:151], v12 offset:30208
	s_waitcnt lgkmcnt(12)
	v_mfma_f32_32x32x16_bf16 v[96:111], v[176:179], v[120:123], v[96:111]
	v_add_f32_e32 v2, v78, v2
	v_add_f32_e32 v2, v79, v2
	v_add_f32_e32 v2, v48, v2
	v_add_f32_e32 v2, v49, v2
	v_cvt_pk_bf16_f32 v138, v76, v77
	v_cvt_pk_bf16_f32 v139, v78, v79
	ds_read_b64_tr_b16 v[176:177], v12 offset:26624
	ds_read_b64_tr_b16 v[178:179], v12 offset:27136
	s_waitcnt lgkmcnt(13)
	v_mfma_f32_32x32x16_bf16 v[80:95], v[172:175], v[116:119], v[80:95]
	v_add_f32_e32 v2, v50, v2
	v_add_f32_e32 v2, v51, v2
	v_add_f32_e32 v2, v52, v2
	v_add_f32_e32 v6, v53, v2
	v_cvt_pk_bf16_f32 v132, v48, v49
	v_cvt_pk_bf16_f32 v133, v50, v51
	ds_read_b64_tr_b16 v[2:3], v12 offset:30720
	ds_read_b64_tr_b16 v[4:5], v12 offset:31232
	s_waitcnt lgkmcnt(14)
	v_mfma_f32_32x32x16_bf16 v[96:111], v[164:167], v[116:119], v[96:111]
	v_add_f32_e32 v6, v54, v6
	v_add_f32_e32 v6, v55, v6
	v_add_f32_e32 v6, v56, v6
	v_add_f32_e32 v10, v57, v6
	v_cvt_pk_bf16_f32 v134, v52, v53
	v_cvt_pk_bf16_f32 v135, v54, v55
	ds_read_b64_tr_b16 v[6:7], v12 offset:27648
	ds_read_b64_tr_b16 v[8:9], v12 offset:28160
	s_waitcnt lgkmcnt(14)
	v_mfma_f32_32x32x16_bf16 v[80:95], v[168:171], v[112:115], v[80:95]
	v_add_f32_e32 v10, v58, v10
	v_add_f32_e32 v10, v59, v10
	v_add_f32_e32 v10, v60, v10
	v_add_f32_e32 v15, v61, v10
	v_cvt_pk_bf16_f32 v128, v56, v57
	v_cvt_pk_bf16_f32 v129, v58, v59
	ds_read_b64_tr_b16 v[10:11], v12 offset:31744
	ds_read_b64_tr_b16 v[12:13], v12 offset:32256
	v_mfma_f32_32x32x16_bf16 v[96:111], v[160:163], v[112:115], v[96:111]
	v_add_f32_e32 v15, v62, v15
	v_add_f32_e32 v15, v63, v15
	v_cvt_pk_bf16_f32 v130, v60, v61
	v_cvt_pk_bf16_f32 v131, v62, v63
	v_lshl_add_u64 v[48:49], v[186:187], 0, s[22:23]
	s_add_i32 s29, s57, s63
	s_mov_b32 m0, s29
	s_nop 0
	global_load_lds_dwordx4 v[48:49], off
	v_lshl_add_u64 v[48:49], v[188:189], 0, s[70:71]
	s_add_i32 s29, s65, s62
	s_mov_b32 m0, s29
	s_nop 0
	global_load_lds_dwordx4 v[48:49], off
	s_waitcnt vmcnt(7)
	v_mul_f32_e32 v48, v201, v191
	v_cmp_nge_f32_e32 vcc, s73, v48
	v_cmp_neq_f32_e64 s[38:39], 0, v207
	s_or_b64 vcc, vcc, s[38:39]
	s_cmp_lg_u64 vcc, 0
	s_cselect_b64 s[38:39], -1, 0
	s_cbranch_vccz .LBB0_1084
	v_sub_f32_e32 v95, v95, v207
	v_sub_f32_e32 v94, v94, v207
	v_sub_f32_e32 v93, v93, v207
	v_sub_f32_e32 v92, v92, v207
	v_sub_f32_e32 v91, v91, v207
	v_sub_f32_e32 v90, v90, v207
	v_sub_f32_e32 v89, v89, v207
	v_sub_f32_e32 v88, v88, v207
	v_sub_f32_e32 v87, v87, v207
	v_sub_f32_e32 v86, v86, v207
	v_sub_f32_e32 v85, v85, v207
	v_sub_f32_e32 v84, v84, v207
	v_sub_f32_e32 v83, v83, v207
	v_sub_f32_e32 v82, v82, v207
	v_sub_f32_e32 v81, v81, v207
	v_sub_f32_e32 v80, v80, v207
	v_sub_f32_e32 v111, v111, v207
	v_sub_f32_e32 v110, v110, v207
	v_sub_f32_e32 v109, v109, v207
	v_sub_f32_e32 v108, v108, v207
	v_sub_f32_e32 v107, v107, v207
	v_sub_f32_e32 v106, v106, v207
	v_sub_f32_e32 v105, v105, v207
	v_sub_f32_e32 v104, v104, v207
	v_sub_f32_e32 v103, v103, v207
	v_sub_f32_e32 v102, v102, v207
	v_sub_f32_e32 v101, v101, v207
	v_sub_f32_e32 v100, v100, v207
	v_sub_f32_e32 v99, v99, v207
	v_sub_f32_e32 v98, v98, v207
	v_sub_f32_e32 v97, v97, v207
	v_sub_f32_e32 v96, v96, v207

.LBB0_1238:
	s_add_i32 s41, s29, -16
	s_min_i32 s41, s41, s1
	s_sub_i32 s40, s29, 32
	s_ashr_i32 s43, s41, 31
	s_add_u32 s42, s17, s41
	s_addc_u32 s43, 0, s43
	s_lshl_b64 s[42:43], s[42:43], 12
	s_waitcnt vmcnt(7) lgkmcnt(0)
	v_mfma_f32_32x32x16_bf16 v[2:17], v[18:21], v[50:53], 0
	v_lshl_add_u64 v[50:51], v[100:101], 0, s[42:43]
	global_load_dwordx4 v[94:97], v[50:51], off
	global_load_dwordx4 v[90:93], v[50:51], off offset:1024
	global_load_dwordx4 v[86:89], v[50:51], off offset:2048
	global_load_dwordx4 v[82:85], v[50:51], off offset:3072
	s_cmp_lt_i32 s40, s1
	s_waitcnt vmcnt(10)
	v_mfma_f32_32x32x16_bf16 v[2:17], v[26:29], v[62:65], v[2:17]
	s_waitcnt vmcnt(7)
	v_mfma_f32_32x32x16_bf16 v[2:17], v[30:33], v[58:61], v[2:17]
	s_waitcnt vmcnt(6)
	v_mfma_f32_32x32x16_bf16 v[2:17], v[34:37], v[54:57], v[2:17]
	s_add_i32 s41, s29, -8
	s_min_i32 s41, s41, s1
	s_ashr_i32 s43, s41, 31
	s_add_u32 s42, s17, s41
	s_addc_u32 s43, 0, s43
	s_lshl_b64 s[42:43], s[42:43], 12
	v_lshl_add_u64 v[54:55], v[100:101], 0, s[42:43]
	global_load_dwordx4 v[50:53], v[54:55], off
	global_load_dwordx4 v[62:65], v[54:55], off offset:1024
	global_load_dwordx4 v[58:61], v[54:55], off offset:2048
	s_nop 0
	global_load_dwordx4 v[54:57], v[54:55], off offset:3072
	s_cmp_lt_i32 s40, s1
	s_nop 1
	v_med3_f32 v2, v2, 0, v233
	v_med3_f32 v10, v10, 0, v233
	v_mul_f32_e32 v2, v22, v2
	v_mul_f32_e32 v10, v42, v10
	v_med3_f32 v3, v3, 0, v233
	v_fmac_f32_e32 v2, v23, v3
	v_med3_f32 v11, v11, 0, v233
	v_fmac_f32_e32 v10, v43, v11
	v_med3_f32 v3, v4, 0, v233
	v_fmac_f32_e32 v2, v24, v3
	v_med3_f32 v4, v12, 0, v233
	v_fmac_f32_e32 v10, v44, v4
	v_med3_f32 v3, v5, 0, v233
	v_fmac_f32_e32 v2, v25, v3
	v_med3_f32 v4, v13, 0, v233
	v_fmac_f32_e32 v10, v45, v4
	v_med3_f32 v3, v6, 0, v233
	v_fmac_f32_e32 v2, v38, v3
	v_med3_f32 v4, v14, 0, v233
	v_fmac_f32_e32 v10, v46, v4
	v_med3_f32 v3, v7, 0, v233
	v_fmac_f32_e32 v2, v39, v3
	v_med3_f32 v4, v15, 0, v233
	v_fmac_f32_e32 v10, v47, v4
	v_med3_f32 v3, v8, 0, v233
	v_fmac_f32_e32 v2, v40, v3
	v_med3_f32 v4, v16, 0, v233
	v_fmac_f32_e32 v10, v48, v4
	v_med3_f32 v3, v9, 0, v233
	v_fmac_f32_e32 v2, v41, v3
	v_med3_f32 v4, v17, 0, v233
	v_fmac_f32_e32 v10, v49, v4
	v_ashrrev_i32_e32 v3, 31, v2
	v_bitop3_b32 v112, v3, v2, s97 bitop3:0x36
	v_ashrrev_i32_e32 v2, 31, v10
	v_bitop3_b32 v113, v2, v10, s97 bitop3:0x36
	s_cbranch_scc1 .LBB0_1240
	v_cmp_le_i32_e32 vcc, v110, v109
	s_nop 1
	v_cndmask_b32_e32 v113, 0, v113, vcc
	v_cmp_le_i32_e32 vcc, v110, v108
	s_nop 1
	v_cndmask_b32_e32 v112, 0, v112, vcc
.LBB0_1240:
	v_mfma_f32_32x32x16_bf16 v[2:17], v[18:21], v[78:81], 0
	s_add_i32 s40, s40, 8
	s_cmp_lt_i32 s40, s1
	ds_write_b32 v111, v112
	v_mfma_f32_32x32x16_bf16 v[2:17], v[26:29], v[70:73], v[2:17]
	v_add_u32_e32 v70, 0x10000, v111
	ds_write_b32 v70, v113
	s_waitcnt vmcnt(9)
	v_mfma_f32_32x32x16_bf16 v[2:17], v[30:33], v[74:77], v[2:17]
	s_waitcnt vmcnt(8)
	v_mfma_f32_32x32x16_bf16 v[2:17], v[34:37], v[66:69], v[2:17]
	s_min_i32 s41, s29, s1
	s_ashr_i32 s43, s41, 31
	s_add_u32 s42, s17, s41
	s_addc_u32 s43, 0, s43
	s_lshl_b64 s[42:43], s[42:43], 12
	v_lshl_add_u64 v[66:67], v[100:101], 0, s[42:43]
	global_load_dwordx4 v[78:81], v[66:67], off
	global_load_dwordx4 v[70:73], v[66:67], off offset:1024
	global_load_dwordx4 v[74:77], v[66:67], off offset:2048
	s_nop 0
	global_load_dwordx4 v[66:69], v[66:67], off offset:3072
	s_cmp_lt_i32 s40, s1
	s_nop 1
	v_med3_f32 v2, v2, 0, v233
	v_med3_f32 v10, v10, 0, v233
	v_mul_f32_e32 v2, v22, v2
	v_med3_f32 v3, v3, 0, v233
	v_mul_f32_e32 v10, v42, v10
	v_fmac_f32_e32 v2, v23, v3
	v_med3_f32 v3, v4, 0, v233
	v_med3_f32 v11, v11, 0, v233
	v_fmac_f32_e32 v10, v43, v11
	v_fmac_f32_e32 v2, v24, v3
	v_med3_f32 v3, v5, 0, v233
	v_med3_f32 v4, v12, 0, v233
	v_fmac_f32_e32 v10, v44, v4
	v_fmac_f32_e32 v2, v25, v3
	v_med3_f32 v3, v6, 0, v233
	v_med3_f32 v4, v13, 0, v233
	v_fmac_f32_e32 v10, v45, v4
	v_fmac_f32_e32 v2, v38, v3
	v_med3_f32 v3, v7, 0, v233
	v_med3_f32 v4, v14, 0, v233
	v_fmac_f32_e32 v10, v46, v4
	v_fmac_f32_e32 v2, v39, v3
	v_med3_f32 v3, v8, 0, v233
	v_med3_f32 v4, v15, 0, v233
	v_fmac_f32_e32 v10, v47, v4
	v_fmac_f32_e32 v2, v40, v3
	v_med3_f32 v3, v9, 0, v233
	v_med3_f32 v4, v16, 0, v233
	v_fmac_f32_e32 v10, v48, v4
	v_fmac_f32_e32 v2, v41, v3
	v_med3_f32 v4, v17, 0, v233
	v_ashrrev_i32_e32 v3, 31, v2
	v_fmac_f32_e32 v10, v49, v4
	v_bitop3_b32 v2, v3, v2, s97 bitop3:0x36
	s_nop 0
	v_ashrrev_i32_e32 v3, 31, v10
	v_bitop3_b32 v3, v3, v10, s97 bitop3:0x36
	s_cbranch_scc1 .LBB0_1242
	v_add_u32_e32 v4, 0x100, v110
	v_cmp_le_i32_e32 vcc, v4, v109
	s_nop 1
	v_cndmask_b32_e32 v3, 0, v3, vcc
	v_cmp_le_i32_e32 vcc, v4, v108
	s_nop 1
	v_cndmask_b32_e32 v2, 0, v2, vcc

.LBB0_1244:
	s_waitcnt vmcnt(11)
	v_mfma_f32_32x32x16_bf16 v[2:17], v[18:21], v[94:97], 0
	s_add_i32 s40, s40, 8
	s_cmp_lt_i32 s40, s1
	s_waitcnt vmcnt(10)
	v_mfma_f32_32x32x16_bf16 v[2:17], v[26:29], v[90:93], v[2:17]
	s_waitcnt vmcnt(9)
	v_mfma_f32_32x32x16_bf16 v[2:17], v[30:33], v[86:89], v[2:17]
	s_waitcnt vmcnt(8)
	v_mfma_f32_32x32x16_bf16 v[2:17], v[34:37], v[82:85], v[2:17]
	s_nop 11
	v_med3_f32 v2, v2, 0, v233
	v_med3_f32 v10, v10, 0, v233
	v_mul_f32_e32 v2, v22, v2
	v_med3_f32 v3, v3, 0, v233
	v_mul_f32_e32 v10, v42, v10
	v_fmac_f32_e32 v2, v23, v3
	v_med3_f32 v3, v4, 0, v233
	v_med3_f32 v11, v11, 0, v233
	v_fmac_f32_e32 v10, v43, v11
	v_fmac_f32_e32 v2, v24, v3
	v_med3_f32 v3, v5, 0, v233
	v_med3_f32 v4, v12, 0, v233
	v_fmac_f32_e32 v10, v44, v4
	v_fmac_f32_e32 v2, v25, v3
	v_med3_f32 v3, v6, 0, v233
	v_med3_f32 v4, v13, 0, v233
	v_fmac_f32_e32 v10, v45, v4
	v_fmac_f32_e32 v2, v38, v3
	v_med3_f32 v3, v7, 0, v233
	v_med3_f32 v4, v14, 0, v233
	v_fmac_f32_e32 v10, v46, v4
	v_fmac_f32_e32 v2, v39, v3
	v_med3_f32 v3, v8, 0, v233
	v_med3_f32 v4, v15, 0, v233
	v_fmac_f32_e32 v10, v47, v4
	v_fmac_f32_e32 v2, v40, v3
	v_med3_f32 v3, v9, 0, v233
	v_med3_f32 v4, v16, 0, v233
	v_fmac_f32_e32 v10, v48, v4
	v_fmac_f32_e32 v2, v41, v3
	v_med3_f32 v4, v17, 0, v233
	v_ashrrev_i32_e32 v3, 31, v2
	v_fmac_f32_e32 v10, v49, v4
	v_bitop3_b32 v2, v3, v2, s97 bitop3:0x36
	s_nop 0
	v_ashrrev_i32_e32 v3, 31, v10
	v_bitop3_b32 v3, v3, v10, s97 bitop3:0x36
	s_cbranch_scc1 .LBB0_1246
	v_add_u32_e32 v4, 0x200, v110
	v_cmp_le_i32_e32 vcc, v4, v109
	s_nop 1
	v_cndmask_b32_e32 v3, 0, v3, vcc
	v_cmp_le_i32_e32 vcc, v4, v108
	s_nop 1
	v_cndmask_b32_e32 v2, 0, v2, vcc
